# baseline (speedup 1.0000x reference)
_Z6k_gemmPKfS0_PK15HIP_vector_typeIjLj4EEPDF16_PKh:
	s_load_dwordx4 s[20:23], s[0:1], 0x0
	s_load_dwordx4 s[4:7], s[0:1], 0x10
	s_load_dwordx2 s[38:39], s[0:1], 0x20
	v_readfirstlane_b32 s8, v0
	v_and_b32_e32 v1, 63, v0
	s_nop 3
	s_lshr_b32 s8, s8, 6
	s_and_b32 s40, s2, 7
	s_lshr_b32 s41, s2, 3
	s_mul_i32 s18, s40, 0x187
	s_add_u32 s19, s18, 0x187
	s_min_u32 s19, s19, 0xc35
	s_sub_u32 s33, s19, s18
	s_sub_u32 s33, s33, 0x180
	s_lshl_b32 s33, s33, 2
	s_cmp_lt_u32 s41, s33
	s_cselect_b32 s44, 7, 6
	s_lshr_b32 s45, s41, 2
	s_add_u32 s45, s45, s18
	s_add_u32 s45, s45, 0x180
	s_lshl_b32 s45, s45, 4
	s_and_b32 s46, s41, 3
	s_lshl_b32 s46, s46, 2
	s_add_u32 s47, s45, s46
	s_mul_i32 s45, s47, 0x4b0
	s_lshl_b32 s46, s47, 8
	s_add_i32 s18, s18, s41
	s_cmp_eq_u32 s8, 0
	s_cselect_b32 s9, s44, 6
	s_add_i32 s11, s44, 4
	s_lshl_b32 s18, s18, 4
	s_lshl_b32 s19, s8, 2
	s_add_i32 s33, s18, s19
	s_mul_i32 s12, s33, 0x4b0
	s_lshl_b32 s32, s18, 8
	s_sub_u32 s32, s32, 0x100000
	s_mov_b32 s10, 0
	v_lshl_add_u32 v253, v1, 10, s33
	v_mov_b32_e32 v254, s47
	v_cmp_eq_u32_e32 vcc, 6, v1
	s_nop 1
	v_cndmask_b32_e32 v253, v253, v254, vcc
	v_mov_b32_e32 v247, 0
	v_cmp_gt_i32_e32 vcc, s9, v1
	s_mov_b32 s18, 0xc350
	v_cmp_gt_i32_e64 s[36:37], s18, v253
	s_and_b64 vcc, vcc, s[36:37]
	s_waitcnt lgkmcnt(0)
	s_and_saveexec_b64 s[36:37], vcc
	global_load_dword v247, v253, s[38:39]
	s_mov_b64 exec, s[36:37]
	s_mov_b32 s24, s22
	s_and_b32 s25, s23, 0xffff
	s_mov_b32 s26, 0x3938700
	s_mov_b32 s27, 0x20000
	s_and_b32 s21, s21, 0xffff
	s_mov_b32 s22, 0x3938700
	s_mov_b32 s23, 0x20000
	s_mov_b32 s28, s6
	s_and_b32 s29, s7, 0xffff
	s_mov_b32 s30, 0xc35000
	s_mov_b32 s31, 0x20000
	v_lshlrev_b32_e32 v238, 4, v1
	v_mul_u32_u24_e32 v253, 0x1746, v1
	v_lshrrev_b32_e32 v253, 16, v253
	v_min_u32_e32 v253, 3, v253
	v_mul_u32_u24_e32 v254, 11, v253
	v_sub_u32_e32 v254, v1, v254
	v_lshlrev_b32_e32 v240, 3, v253
	v_mul_u32_u24_e32 v249, 0x4b0, v253
	v_lshl_add_u32 v249, v254, 4, v249
	v_add_u32_e32 v249, 0x400, v249
	v_mov_b32_e32 v255, 0x80000000
	v_cmp_gt_u32_e64 s[34:35], 44, v1
	s_nop 1
	v_cndmask_b32_e64 v239, v255, v249, s[34:35]
	v_lshl_add_u32 v250, s8, 2, v253
	v_mul_u32_u24_e32 v250, 0x4e0, v250
	v_lshl_add_u32 v250, v254, 3, v250
	v_add_u32_e32 v242, 0x200, v250
	s_mul_i32 s18, s8, 0x1380
	v_lshl_add_u32 v241, v1, 3, s18
	v_and_b32_e32 v249, 15, v1
	v_lshrrev_b32_e32 v250, 4, v1
	v_mul_u32_u24_e32 v243, 0x4e0, v249
	v_lshl_add_u32 v243, v250, 4, v243
	v_mul_u32_u24_e32 v244, 0x440, v250
	v_lshl_add_u32 v244, v249, 1, v244
	s_lshl_b32 s18, s8, 6
	s_add_i32 s18, s18, 39936
	v_add_u32_e32 v244, s18, v244
	v_lshrrev_b32_e32 v249, 4, v0
	v_and_b32_e32 v250, 15, v0
	v_mul_u32_u24_e32 v245, 0x110, v249
	v_lshl_add_u32 v245, v250, 4, v245
	v_add_u32_e32 v245, 39936, v245
	v_lshlrev_b32_e32 v246, 8, v249
	v_lshl_add_u32 v246, v250, 4, v246
	s_lshl_b32 s18, s8, 12
	s_add_i32 s18, s18, 48640
	v_lshl_add_u32 v248, v1, 4, s18
	v_cmp_gt_u32_e32 vcc, 32, v0
	s_and_saveexec_b64 s[36:37], vcc
	v_mul_u32_u24_e32 v251, 0x4e00, v249
	v_mul_u32_u24_e32 v252, 0x4e0, v250
	v_add_u32_e32 v254, v251, v252
	v_mov_b32_e32 v250, 0
	v_mov_b32_e32 v251, 0
	v_mov_b32_e32 v252, 0
	v_mov_b32_e32 v253, 0
	ds_write_b128 v254, v[250:253] offset:1200
	s_mov_b64 exec, s[36:37]
	s_lshl_b32 s18, s8, 11
	v_lshl_add_u32 v253, v1, 4, s18
	v_add_u32_e32 v254, 0x22000, v253
	global_load_dwordx4 v[178:181], v254, s[4:5]
	global_load_dwordx4 v[182:185], v254, s[4:5] offset:1024
	v_add_u32_e32 v254, 0x2000, v254
	global_load_dwordx4 v[186:189], v254, s[4:5]
	global_load_dwordx4 v[190:193], v254, s[4:5] offset:1024
	v_mov_b32_e32 v236, v253
	s_waitcnt vmcnt(4)
	v_readlane_b32 s13, v247, s10
	s_add_u32 s14, s12, 0x4b0
	s_add_u32 s15, s12, 0x960
	s_add_u32 s16, s12, 0xe10
	s_nop 1
	s_and_b32 s18, s13, 0xff
	s_cmp_eq_u32 s18, 1
	s_cselect_b32 s42, s12, 0x80000000
	s_and_b32 s18, s13, 0xff00
	s_cmp_eq_u32 s18, 0x100
	s_cselect_b32 s14, s14, 0x80000000
	s_and_b32 s18, s13, 0xff0000
	s_cmp_eq_u32 s18, 0x10000
	s_cselect_b32 s15, s15, 0x80000000
	s_and_b32 s18, s13, 0xff000000
	s_cmp_eq_u32 s18, 0x1000000
	s_cselect_b32 s16, s16, 0x80000000
	v_lshrrev_b32_e64 v249, v240, s13
	v_and_b32_e32 v249, 0xff, v249
	v_cmp_eq_u32_e32 vcc, 1, v249
	s_nop 1
	v_cndmask_b32_e32 v254, v255, v239, vcc
	buffer_load_dwordx4 v[138:141], v238, s[20:23], s42 offen sc1 nt
	buffer_load_dwordx4 v[142:145], v238, s[24:27], s42 offen sc1 nt
	buffer_load_dwordx4 v[146:149], v238, s[20:23], s14 offen sc1 nt
	buffer_load_dwordx4 v[150:153], v238, s[24:27], s14 offen sc1 nt
	buffer_load_dwordx4 v[154:157], v238, s[20:23], s15 offen sc1 nt
	buffer_load_dwordx4 v[158:161], v238, s[24:27], s15 offen sc1 nt
	buffer_load_dwordx4 v[162:165], v238, s[20:23], s16 offen sc1 nt
	buffer_load_dwordx4 v[166:169], v238, s[24:27], s16 offen sc1 nt
	buffer_load_dwordx4 v[170:173], v254, s[20:23], s12 offen sc1 nt
	buffer_load_dwordx4 v[174:177], v254, s[24:27], s12 offen sc1 nt
	s_add_u32 s12, s12, 0x12c000
	s_add_u32 s32, s32, 0x40000
	s_mov_b32 s19, 0x80000000
	buffer_store_dwordx4 v[226:229], v246, s[28:31], s19 offen sc0 sc1
	s_mov_b32 s10, 1
	global_load_dwordx4 v[2:5], v236, s[4:5]
	global_load_dwordx4 v[6:9], v236, s[4:5] offset:1024
	v_add_u32_e32 v236, 0x2000, v236
	global_load_dwordx4 v[10:13], v236, s[4:5]
	global_load_dwordx4 v[14:17], v236, s[4:5] offset:1024
	v_add_u32_e32 v236, 0x2000, v236
	global_load_dwordx4 v[18:21], v236, s[4:5]
	global_load_dwordx4 v[22:25], v236, s[4:5] offset:1024
	v_add_u32_e32 v236, 0x2000, v236
	global_load_dwordx4 v[26:29], v236, s[4:5]
	global_load_dwordx4 v[30:33], v236, s[4:5] offset:1024
	v_add_u32_e32 v236, 0x2000, v236
	global_load_dwordx4 v[34:37], v236, s[4:5]
	global_load_dwordx4 v[38:41], v236, s[4:5] offset:1024
	v_add_u32_e32 v236, 0x2000, v236
	global_load_dwordx4 v[42:45], v236, s[4:5]
	global_load_dwordx4 v[46:49], v236, s[4:5] offset:1024
	v_add_u32_e32 v236, 0x2000, v236
	global_load_dwordx4 v[50:53], v236, s[4:5]
	global_load_dwordx4 v[54:57], v236, s[4:5] offset:1024
	v_add_u32_e32 v236, 0x2000, v236
	global_load_dwordx4 v[58:61], v236, s[4:5]
	global_load_dwordx4 v[62:65], v236, s[4:5] offset:1024
	v_add_u32_e32 v236, 0x2000, v236
	global_load_dwordx4 v[66:69], v236, s[4:5]
	global_load_dwordx4 v[70:73], v236, s[4:5] offset:1024
	v_add_u32_e32 v236, 0x2000, v236
	global_load_dwordx4 v[74:77], v236, s[4:5]
	global_load_dwordx4 v[78:81], v236, s[4:5] offset:1024
	v_add_u32_e32 v236, 0x2000, v236
	global_load_dwordx4 v[82:85], v236, s[4:5]
	global_load_dwordx4 v[86:89], v236, s[4:5] offset:1024
	v_add_u32_e32 v236, 0x2000, v236
	global_load_dwordx4 v[90:93], v236, s[4:5]
	global_load_dwordx4 v[94:97], v236, s[4:5] offset:1024
	v_add_u32_e32 v236, 0x2000, v236
	global_load_dwordx4 v[98:101], v236, s[4:5]
	global_load_dwordx4 v[102:105], v236, s[4:5] offset:1024
	v_add_u32_e32 v236, 0x2000, v236
	global_load_dwordx4 v[106:109], v236, s[4:5]
	global_load_dwordx4 v[110:113], v236, s[4:5] offset:1024
	v_add_u32_e32 v236, 0x2000, v236
	global_load_dwordx4 v[114:117], v236, s[4:5]
	global_load_dwordx4 v[118:121], v236, s[4:5] offset:1024
	v_add_u32_e32 v236, 0x2000, v236
	global_load_dwordx4 v[122:125], v236, s[4:5]
	global_load_dwordx4 v[126:129], v236, s[4:5] offset:1024
	v_add_u32_e32 v236, 0x2000, v236
	global_load_dwordx4 v[130:133], v236, s[4:5]
	global_load_dwordx4 v[134:137], v236, s[4:5] offset:1024
	s_waitcnt vmcnt(45)
	ds_write_b128 v248, v[178:181]
	ds_write_b128 v248, v[182:185] offset:1024
	ds_write_b128 v248, v[186:189] offset:2048
	ds_write_b128 v248, v[190:193] offset:3072
	s_waitcnt lgkmcnt(0)
	s_barrier
	s_branch .Lg_half1
	.p2align	6

.Lg_s3skip0:
	s_cmp_eq_u32 s10, 10
	s_cselect_b32 s32, s46, s32
	s_sub_u32 s18, s10, 4
	s_cmp_lt_u32 s18, s9
	s_cselect_b32 s19, s32, 0x80000000
	ds_read_b128 v[226:229], v245 offset:0
	s_add_u32 s32, s32, 0x40000
	v_readlane_b32 s13, v247, s18
	v_lshrrev_b32_e32 v249, 4, v1
	v_lshlrev_b32_e32 v249, 3, v249
	v_lshrrev_b32_e64 v249, v249, s13
	v_and_b32_e32 v249, 0xff, v249
	v_cmp_eq_u32_e32 vcc, 1, v249
	s_nop 1
	v_cndmask_b32_e32 v249, v255, v246, vcc
	s_waitcnt lgkmcnt(0)
	buffer_store_dwordx4 v[226:229], v249, s[28:31], s19 offen sc0 sc1
	s_add_u32 s10, s10, 1
	s_cmp_ge_u32 s10, s11
	s_cbranch_scc1 .Lg_end
	s_barrier
	s_cmp_ge_u32 s10, s11
	s_cbranch_scc1 .Lg_end
	.p2align	6
